# stage1b
# speedup vs baseline: 1.0057x; 1.0057x over previous
_Z11attn_kernelILi4EEvPKfS1_S1_S1_S1_S1_PKcPf:
	s_load_dwordx2 s[24:25], s[0:1], 0x30
	s_load_dwordx8 s[8:15], s[0:1], 0x0
	s_load_dwordx4 s[16:19], s[0:1], 0x20
	v_lshrrev_b32_e32 v63, 6, v0
	v_and_b32_e32 v104, 63, v0
	v_mad_u32_u24 v2, v63, 12, v104
	v_cmp_gt_u32_e32 vcc, 12, v104
	v_and_b32_e32 v57, 15, v0
	v_bfe_u32 v1, v0, 4, 2
	v_cndmask_b32_e32 v2, 48, v2, vcc
	v_lshlrev_b32_e32 v2, 2, v2
	v_lshlrev_b32_e32 v60, 5, v57
	v_lshlrev_b32_e32 v58, 3, v1
	v_add_u32_e32 v3, v60, v58
	v_lshrrev_b32_e32 v56, 4, v0
	v_lshlrev_b32_e32 v54, 4, v57
	v_mov_b32_e32 v59, 0
	s_movk_i32 s4, 0xe0
	v_cmp_gt_u32_e64 s[4:5], s4, v0
	s_lshl_b32 s26, s2, 8
	s_lshl_b32 s27, s2, 9
	s_mul_i32 s28, s2, 14
	v_lshlrev_b32_e32 v5, 2, v57
	v_lshlrev_b32_e32 v147, 6, v57
	s_waitcnt lgkmcnt(0)
	s_add_u32 s20, s24, s26
	s_addc_u32 s21, s25, 0
	s_add_u32 s20, s20, 0x164000
	s_addc_u32 s21, s21, 0
	s_add_u32 s26, s24, s27
	s_addc_u32 s27, s25, 0
	s_add_u32 s26, s26, 0x80000
	s_addc_u32 s27, s27, 0
	global_load_dword v61, v2, s[20:21]
	global_load_dwordx2 v[64:65], v3, s[26:27]
	s_add_u32 s22, s24, 0x160000
	s_addc_u32 s23, s25, 0
	v_cndmask_b32_e64 v62, 13, v56, s[4:5]
	v_add_u32_e32 v3, s28, v62
	v_mad_u32_u24 v144, v3, 36, v5
	v_mad_u32_u24 v146, v3, 12, v5
	v_add_u32_e32 v145, -36, v146
	v_add_u32_e32 v146, -48, v146
	v_lshl_or_b32 v147, v63, 10, v147
	v_lshl_or_b32 v147, v1, 4, v147
	v_or_b32_e32 v148, 0x1000, v147
	v_lshlrev_b32_e32 v149, 4, v104
	v_lshlrev_b32_e32 v150, 9, v3
	v_add_u32_e32 v150, v150, v54
	s_waitcnt vmcnt(1)
	v_readlane_b32 s3, v61, 12
	s_bitcmp0_b32 s3, 1
	s_cselect_b64 s[20:21], -1, 0
	s_cbranch_scc1 .LBB1_16
	v_mbcnt_lo_u32_b32 v3, -1, 0
	v_mbcnt_hi_u32_b32 v3, -1, v3
	v_lshrrev_b32_e32 v2, 2, v57
	v_and_b32_e32 v20, 64, v3
	v_or_b32_e32 v2, v20, v2
	v_lshlrev_b32_e32 v3, 2, v2
	ds_bpermute_b32 v2, v3, v61
	ds_bpermute_b32 v4, v3, v61 offset:16
	ds_bpermute_b32 v6, v3, v61 offset:32
	v_lshlrev_b32_e32 v8, 6, v1
	v_mov_b32_e32 v9, v59
	v_lshlrev_b32_e32 v3, 4, v0
	v_lshl_add_u64 v[8:9], s[24:25], 0, v[8:9]
	v_and_b32_e32 v10, 48, v3
	v_mov_b32_e32 v11, v59
	s_waitcnt lgkmcnt(0)
	v_ashrrev_i32_e32 v3, 31, v2
	v_lshl_add_u64 v[8:9], v[8:9], 0, v[10:11]
	v_lshlrev_b64 v[2:3], 9, v[2:3]
	v_lshl_add_u64 v[2:3], v[8:9], 0, v[2:3]
	v_ashrrev_i32_e32 v5, 31, v4
	global_load_dwordx4 v[50:53], v[2:3], off
	global_load_dwordx4 v[46:49], v[2:3], off offset:256
	v_lshlrev_b64 v[2:3], 9, v[4:5]
	v_lshl_add_u64 v[2:3], v[8:9], 0, v[2:3]
	v_ashrrev_i32_e32 v7, 31, v6
	global_load_dwordx4 v[14:17], v[2:3], off
	global_load_dwordx4 v[10:13], v[2:3], off offset:256
	v_lshlrev_b64 v[2:3], 9, v[6:7]
	v_lshl_add_u64 v[18:19], v[8:9], 0, v[2:3]
	global_load_dwordx4 v[6:9], v[18:19], off
	global_load_dwordx4 v[2:5], v[18:19], off offset:256
	v_or_b32_e32 v18, v20, v1
	v_lshlrev_b32_e32 v19, 2, v18
	ds_bpermute_b32 v18, v19, v61
	ds_bpermute_b32 v20, v19, v61 offset:16
	ds_bpermute_b32 v22, v19, v61 offset:32
	s_add_u32 s26, s24, 0x140000
	s_addc_u32 s27, s25, 0
	v_mov_b32_e32 v55, v59
	s_waitcnt lgkmcnt(2)
	v_ashrrev_i32_e32 v19, 31, v18
	v_lshl_add_u64 v[24:25], s[24:25], 0, v[54:55]
	s_mov_b64 s[24:25], 0x100000
	v_lshlrev_b64 v[26:27], 8, v[18:19]
	v_lshl_or_b32 v18, v18, 4, v57
	v_lshl_add_u64 v[24:25], v[24:25], 0, s[24:25]
	v_ashrrev_i32_e32 v19, 31, v18
	v_lshl_add_u64 v[26:27], v[24:25], 0, v[26:27]
	v_lshl_add_u64 v[18:19], v[18:19], 3, s[26:27]
	s_waitcnt lgkmcnt(1)
	v_ashrrev_i32_e32 v21, 31, v20
	global_load_dwordx4 v[30:33], v[26:27], off
	global_load_dwordx2 v[70:71], v[18:19], off
	v_lshlrev_b64 v[18:19], 8, v[20:21]
	v_lshl_or_b32 v20, v20, 4, v57
	v_lshl_add_u64 v[18:19], v[24:25], 0, v[18:19]
	v_ashrrev_i32_e32 v21, 31, v20
	s_waitcnt lgkmcnt(0)
	v_ashrrev_i32_e32 v23, 31, v22
	v_lshl_add_u64 v[20:21], v[20:21], 3, s[26:27]
	global_load_dwordx4 v[26:29], v[18:19], off
	global_load_dwordx2 v[66:67], v[20:21], off
	v_lshlrev_b64 v[18:19], 8, v[22:23]
	v_lshl_add_u64 v[24:25], v[24:25], 0, v[18:19]
	v_lshl_or_b32 v18, v22, 4, v57
	v_ashrrev_i32_e32 v19, 31, v18
	v_lshl_add_u64 v[22:23], v[18:19], 3, s[26:27]
	global_load_dwordx4 v[18:21], v[24:25], off
	global_load_dwordx2 v[68:69], v[22:23], off
	s_mov_b32 exec_lo, 0x1ff01ff
	s_mov_b32 exec_hi, 0x1ff01ff
	global_load_dword v120, v144, s[10:11]
	s_mov_b32 exec_lo, 0xe000e00
	s_mov_b32 exec_hi, 0xe000e00
	global_load_dword v120, v145, s[12:13]
	s_mov_b32 exec_lo, 0x70007000
	s_mov_b32 exec_hi, 0x70007000
	global_load_dword v120, v146, s[14:15]
	s_mov_b64 exec, -1
	global_load_dwordx4 v[124:127], v147, s[22:23]
	global_load_dwordx4 v[128:131], v148, s[22:23]
	s_mov_b32 exec_hi, 0
	global_load_dwordx4 v[132:135], v149, s[16:17]
	s_mov_b32 exec_hi, -1
	s_mov_b32 exec_lo, 0
	global_load_dwordx4 v[132:135], v149, s[18:19] offset:-512
	s_mov_b32 exec_lo, -1
	global_load_dwordx4 v[136:139], v150, s[8:9]
	global_load_dwordx4 v[140:143], v150, s[8:9] offset:256
	s_movk_i32 s6, 0x140
	v_cmp_gt_u32_e32 vcc, s6, v0
	s_and_saveexec_b64 s[6:7], vcc
	v_lshlrev_b32_e32 v22, 2, v0
	v_mov_b32_e32 v23, 0
	ds_write_b32 v22, v23 offset:14336
	s_or_b64 exec, exec, s[6:7]
	v_cmp_gt_u32_e32 vcc, 64, v0
	s_and_saveexec_b64 s[6:7], vcc
	v_lshlrev_b32_e32 v22, 2, v0
	v_mov_b32_e32 v23, 0
	ds_write_b32 v22, v23 offset:15360
	s_or_b64 exec, exec, s[6:7]
	v_bfe_u32 v22, s3, v57, 1
	v_cmp_eq_u32_e32 vcc, 0, v22
	s_bitcmp0_b32 s3, 0
	v_mov_b32_e32 v45, 0xc9c35000
	v_cndmask_b32_e64 v55, 1.0, 0, vcc
	s_cselect_b64 vcc, -1, 0
	s_bitcmp0_b32 s3, 2
	v_cndmask_b32_e32 v34, 0, v45, vcc
	s_cselect_b64 vcc, -1, 0
	s_bitcmp0_b32 s3, 3
	v_cndmask_b32_e32 v36, 0, v45, vcc
	s_cselect_b64 vcc, -1, 0
	s_bitcmp0_b32 s3, 4
	v_cndmask_b32_e32 v37, 0, v45, vcc
	s_cselect_b64 vcc, -1, 0
	s_bitcmp0_b32 s3, 5
	v_cndmask_b32_e32 v22, 0, v45, vcc
	s_cselect_b64 vcc, -1, 0
	s_bitcmp0_b32 s3, 6
	v_cndmask_b32_e32 v23, 0, v45, vcc
	s_cselect_b64 vcc, -1, 0
	s_bitcmp0_b32 s3, 7
	v_cndmask_b32_e32 v24, 0, v45, vcc
	s_cselect_b64 vcc, -1, 0
	s_bitcmp0_b32 s3, 8
	v_cndmask_b32_e32 v25, 0, v45, vcc
	s_cselect_b64 vcc, -1, 0
	s_bitcmp0_b32 s3, 9
	v_cndmask_b32_e32 v38, 0, v45, vcc
	s_cselect_b64 vcc, -1, 0
	s_bitcmp0_b32 s3, 10
	v_cndmask_b32_e32 v39, 0, v45, vcc
	s_cselect_b64 vcc, -1, 0
	s_bitcmp0_b32 s3, 11
	v_cndmask_b32_e32 v40, 0, v45, vcc
	s_cselect_b64 vcc, -1, 0
	s_bitcmp0_b32 s3, 12
	v_cndmask_b32_e32 v41, 0, v45, vcc
	s_cselect_b64 vcc, -1, 0
	v_mov_b32_e32 v35, 0
	s_bitcmp0_b32 s3, 13
	v_cndmask_b32_e32 v42, 0, v45, vcc
	s_waitcnt vmcnt(20)
	v_mfma_f32_16x16x32_fp8_fp8 v[80:83], v[50:51], v[64:65], v[34:37]
	s_cselect_b64 vcc, -1, 0
	s_bitcmp0_b32 s3, 14
	v_cndmask_b32_e32 v43, 0, v45, vcc
	v_mfma_f32_16x16x32_fp8_fp8 v[84:87], v[52:53], v[64:65], v[22:25]
	s_cselect_b64 vcc, -1, 0
	s_bitcmp0_b32 s3, 15
	v_cndmask_b32_e32 v44, 0, v45, vcc
	s_waitcnt vmcnt(19)
	v_mfma_f32_16x16x32_fp8_fp8 v[88:91], v[46:47], v[64:65], v[38:41]
	s_cselect_b64 vcc, -1, 0
	v_cndmask_b32_e32 v45, 0, v45, vcc
	v_max_f32_e32 v46, v83, v83
	v_max_f32_e32 v47, v82, v82
	v_mfma_f32_16x16x32_fp8_fp8 v[92:95], v[48:49], v[64:65], v[42:45]
	v_max_f32_e32 v46, v47, v46
	v_max_f32_e32 v47, v87, v87
	v_max_f32_e32 v48, v86, v86
	v_max_f32_e32 v47, v48, v47
	v_max_f32_e32 v48, v89, v89
	v_max_f32_e32 v49, v88, v88
	v_max_f32_e32 v48, v49, v48
	v_max_f32_e32 v49, v91, v91
	v_max_f32_e32 v50, v90, v90
	v_max_f32_e32 v49, v50, v49
	v_max_f32_e32 v50, v95, v95
	v_max_f32_e32 v51, v94, v94
	v_max_f32_e32 v50, v51, v50
	v_max3_f32 v50, v92, v93, v50
	v_max3_f32 v46, v80, v81, v46
	v_max3_f32 v47, v84, v85, v47
	v_max3_f32 v48, v48, v49, v50
	v_max3_f32 v46, v46, v47, v48
	v_mul_f32_e32 v47, 0xbdb8aa3b, v46
	v_fmamk_f32 v46, v80, 0x3db8aa3b, v47
	v_fmamk_f32 v49, v88, 0x3db8aa3b, v47
	v_exp_f32_e32 v76, v46
	v_fmamk_f32 v46, v81, 0x3db8aa3b, v47
	v_exp_f32_e32 v77, v49
	v_fmamk_f32 v49, v89, 0x3db8aa3b, v47
	v_exp_f32_e32 v78, v46
	v_fmamk_f32 v46, v82, 0x3db8aa3b, v47
	v_exp_f32_e32 v79, v49
	v_fmamk_f32 v49, v90, 0x3db8aa3b, v47
	v_exp_f32_e32 v52, v46
	v_fmamk_f32 v46, v83, 0x3db8aa3b, v47
	v_exp_f32_e32 v53, v49
	v_fmamk_f32 v49, v91, 0x3db8aa3b, v47
	v_exp_f32_e32 v74, v46
	v_fmamk_f32 v46, v84, 0x3db8aa3b, v47
	v_exp_f32_e32 v75, v49
	v_fmamk_f32 v49, v92, 0x3db8aa3b, v47
	v_exp_f32_e32 v50, v46
	v_fmamk_f32 v46, v85, 0x3db8aa3b, v47
	v_exp_f32_e32 v51, v49
	v_fmamk_f32 v49, v93, 0x3db8aa3b, v47
	v_exp_f32_e32 v72, v46
	v_fmamk_f32 v46, v86, 0x3db8aa3b, v47
	v_exp_f32_e32 v73, v49
	v_fmamk_f32 v49, v94, 0x3db8aa3b, v47
	v_exp_f32_e32 v48, v46
	v_fmamk_f32 v46, v87, 0x3db8aa3b, v47
	v_exp_f32_e32 v49, v49
	v_fmac_f32_e32 v47, 0x3db8aa3b, v95
	v_exp_f32_e32 v46, v46
	v_exp_f32_e32 v47, v47
	v_pk_add_f32 v[96:97], v[76:77], 0 op_sel_hi:[1,0]
	v_pk_add_f32 v[98:99], v[50:51], 0 op_sel_hi:[1,0]
	v_pk_add_f32 v[96:97], v[96:97], v[78:79]
	v_pk_add_f32 v[98:99], v[98:99], v[72:73]
	v_pk_add_f32 v[96:97], v[96:97], v[52:53]
	v_pk_add_f32 v[98:99], v[98:99], v[48:49]
	v_pk_add_f32 v[96:97], v[96:97], v[74:75]
	v_pk_add_f32 v[98:99], v[98:99], v[46:47]
	s_waitcnt vmcnt(17)
	v_mfma_f32_16x16x32_fp8_fp8 v[100:103], v[10:11], v[64:65], v[38:41]
	v_add_f32_e64 v96, v96, v98
	v_add_f32_e64 v97, v97, v99
	s_mov_b32 s6, 0x3d800000
	v_add_f32_e32 v105, v96, v97
	v_mov_b32_e32 v96, v80
	v_mov_b32_e32 v97, v88
	v_pk_fma_f32 v[96:97], v[76:77], v[96:97], 0 op_sel_hi:[1,1,0]
	v_mov_b32_e32 v88, v81
	v_pk_fma_f32 v[80:81], v[78:79], v[88:89], v[96:97]
	v_mov_b32_e32 v88, v82
	v_mov_b32_e32 v89, v90
	v_mov_b32_e32 v90, v83
	v_mov_b32_e32 v82, v84
	v_mov_b32_e32 v83, v92
	v_pk_fma_f32 v[82:83], v[50:51], v[82:83], 0 op_sel_hi:[1,1,0]
	v_mov_b32_e32 v92, v85
	v_pk_fma_f32 v[82:83], v[72:73], v[92:93], v[82:83]
	v_mov_b32_e32 v84, v86
	v_mov_b32_e32 v85, v94
	v_pk_fma_f32 v[82:83], v[48:49], v[84:85], v[82:83]
	v_mov_b32_e32 v94, v87
	v_pk_fma_f32 v[80:81], v[52:53], v[88:89], v[80:81]
	v_mfma_f32_16x16x32_fp8_fp8 v[96:99], v[14:15], v[64:65], v[34:37]
	v_fma_f32 v14, v46, v94, v82
	v_fma_f32 v15, v47, v95, v83
	v_rcp_f32_e32 v82, v105
	v_pk_fma_f32 v[80:81], v[74:75], v[90:91], v[80:81]
	v_mfma_f32_16x16x32_fp8_fp8 v[10:13], v[12:13], v[64:65], v[42:45]
	v_add_f32_e64 v80, v80, v14
	v_add_f32_e64 v81, v81, v15
	v_mul_f32_e32 v110, v55, v82
	v_add_f32_e32 v80, v80, v81
	v_mfma_f32_16x16x32_fp8_fp8 v[14:17], v[16:17], v[64:65], v[22:25]
	v_mul_f32_e32 v111, v80, v110
	v_max_f32_e32 v80, v99, v99
	v_max_f32_e32 v81, v98, v98
	v_max_f32_e32 v80, v81, v80
	v_max_f32_e32 v83, v100, v100
	s_nop 2
	v_max_f32_e32 v81, v17, v17
	v_max_f32_e32 v82, v16, v16
	v_max_f32_e32 v81, v82, v81
	v_max_f32_e32 v82, v101, v101
	v_max_f32_e32 v82, v83, v82
	v_max_f32_e32 v83, v103, v103
	v_max_f32_e32 v84, v102, v102
	v_max_f32_e32 v83, v84, v83
	v_max_f32_e32 v84, v13, v13
	v_max_f32_e32 v85, v12, v12
	v_max_f32_e32 v84, v85, v84
	v_max3_f32 v84, v10, v11, v84
	v_max3_f32 v80, v96, v97, v80
	v_max3_f32 v81, v14, v15, v81
	v_max3_f32 v82, v82, v83, v84
	v_max3_f32 v80, v80, v81, v82
	v_mul_f32_e32 v87, 0xbdb8aa3b, v80
	v_fmamk_f32 v81, v17, 0x3db8aa3b, v87
	v_fmamk_f32 v80, v96, 0x3db8aa3b, v87
	v_exp_f32_e32 v86, v81
	v_fmamk_f32 v81, v100, 0x3db8aa3b, v87
	v_exp_f32_e32 v92, v80
	v_fmamk_f32 v80, v97, 0x3db8aa3b, v87
	v_exp_f32_e32 v93, v81
	v_fmamk_f32 v81, v101, 0x3db8aa3b, v87
	v_exp_f32_e32 v94, v80
	v_fmamk_f32 v80, v98, 0x3db8aa3b, v87
	v_exp_f32_e32 v95, v81
	v_fmamk_f32 v81, v102, 0x3db8aa3b, v87
	v_exp_f32_e32 v84, v80
	v_fmamk_f32 v80, v99, 0x3db8aa3b, v87
	v_exp_f32_e32 v85, v81
	v_fmamk_f32 v81, v103, 0x3db8aa3b, v87
	v_exp_f32_e32 v90, v80
	v_fmamk_f32 v80, v14, 0x3db8aa3b, v87
	v_exp_f32_e32 v91, v81
	v_fmamk_f32 v81, v10, 0x3db8aa3b, v87
	v_exp_f32_e32 v82, v80
	v_fmamk_f32 v80, v15, 0x3db8aa3b, v87
	v_exp_f32_e32 v83, v81
	v_fmamk_f32 v81, v11, 0x3db8aa3b, v87
	v_exp_f32_e32 v88, v80
	v_fmamk_f32 v80, v16, 0x3db8aa3b, v87
	v_exp_f32_e32 v89, v81
	v_fmamk_f32 v81, v12, 0x3db8aa3b, v87
	v_exp_f32_e32 v80, v80
	v_exp_f32_e32 v81, v81
	v_fmac_f32_e32 v87, 0x3db8aa3b, v13
	v_exp_f32_e32 v87, v87
	v_pk_add_f32 v[106:107], v[92:93], 0 op_sel_hi:[1,0]
	v_pk_add_f32 v[108:109], v[82:83], 0 op_sel_hi:[1,0]
	v_pk_add_f32 v[106:107], v[106:107], v[94:95]
	v_pk_add_f32 v[108:109], v[108:109], v[88:89]
	v_pk_add_f32 v[106:107], v[106:107], v[84:85]
	v_pk_add_f32 v[108:109], v[108:109], v[80:81]
	v_pk_add_f32 v[106:107], v[106:107], v[90:91]
	v_pk_add_f32 v[108:109], v[108:109], v[86:87]
	v_mul_f32_e32 v112, 0x3d800000, v111
	v_pk_add_f32 v[106:107], v[106:107], v[108:109]
	v_mul_f32_e32 v105, v105, v110
	v_add_f32_e32 v113, v106, v107
	v_mov_b32_e32 v106, v96
	v_mov_b32_e32 v107, v100
	v_pk_fma_f32 v[106:107], v[92:93], v[106:107], 0 op_sel_hi:[1,1,0]
	v_mov_b32_e32 v100, v97
	v_pk_fma_f32 v[96:97], v[94:95], v[100:101], v[106:107]
	v_mov_b32_e32 v100, v98
	v_mov_b32_e32 v101, v102
	v_mov_b32_e32 v102, v99
	v_mov_b32_e32 v98, v14
	v_mov_b32_e32 v99, v10
	v_pk_fma_f32 v[98:99], v[82:83], v[98:99], 0 op_sel_hi:[1,1,0]
	v_mov_b32_e32 v10, v15
	v_pk_fma_f32 v[10:11], v[88:89], v[10:11], v[98:99]
	v_mov_b32_e32 v14, v16
	v_mov_b32_e32 v15, v12
	v_pk_fma_f32 v[10:11], v[80:81], v[14:15], v[10:11]
	v_mov_b32_e32 v12, v17
	v_pk_fma_f32 v[10:11], v[86:87], v[12:13], v[10:11]
	v_rcp_f32_e32 v12, v113
	v_pk_fma_f32 v[96:97], v[84:85], v[100:101], v[96:97]
	s_waitcnt vmcnt(16)
	v_mfma_f32_16x16x32_fp8_fp8 v[106:109], v[6:7], v[64:65], v[34:37]
	v_fma_f32 v96, v90, v102, v96
	v_fma_f32 v97, v91, v103, v97
	v_mul_f32_e32 v114, v55, v12
	v_pk_add_f32 v[10:11], v[96:97], v[10:11]
	v_mfma_f32_16x16x32_fp8_fp8 v[6:9], v[8:9], v[64:65], v[22:25]
	v_add_f32_e32 v14, v10, v11
	v_mul_f32_e32 v115, v14, v114
	s_nop 0
	v_max_f32_e32 v14, v109, v109
	s_waitcnt vmcnt(15)
	v_mfma_f32_16x16x32_fp8_fp8 v[10:13], v[2:3], v[64:65], v[38:41]
	v_max_f32_e32 v15, v108, v108
	v_max_f32_e32 v14, v15, v14
	v_max_f32_e32 v15, v9, v9
	v_mfma_f32_16x16x32_fp8_fp8 v[2:5], v[4:5], v[64:65], v[42:45]
	v_max_f32_e32 v16, v8, v8
	v_max_f32_e32 v15, v16, v15
	s_nop 1
	v_max_f32_e32 v16, v11, v11
	v_max_f32_e32 v17, v10, v10
	v_max_f32_e32 v16, v17, v16
	v_max_f32_e32 v17, v13, v13
	v_max_f32_e32 v22, v12, v12
	v_max_f32_e32 v17, v22, v17
	v_max_f32_e32 v22, v5, v5
	v_max_f32_e32 v23, v4, v4
	v_max_f32_e32 v22, v23, v22
	v_max3_f32 v22, v2, v3, v22
	v_max3_f32 v14, v106, v107, v14
	v_max3_f32 v15, v6, v7, v15
	v_max3_f32 v16, v16, v17, v22
	v_max3_f32 v14, v14, v15, v16
	v_mul_f32_e32 v14, 0xbdb8aa3b, v14
	v_fmamk_f32 v15, v106, 0x3db8aa3b, v14
	v_exp_f32_e32 v96, v15
	v_fmamk_f32 v15, v107, 0x3db8aa3b, v14
	v_exp_f32_e32 v102, v15
	v_fmamk_f32 v15, v108, 0x3db8aa3b, v14
	v_exp_f32_e32 v44, v15
	v_fmamk_f32 v15, v109, 0x3db8aa3b, v14
	v_exp_f32_e32 v100, v15
	v_fmamk_f32 v15, v6, 0x3db8aa3b, v14
	v_exp_f32_e32 v42, v15
	v_fmamk_f32 v15, v7, 0x3db8aa3b, v14
	v_exp_f32_e32 v98, v15
	v_fmamk_f32 v15, v8, 0x3db8aa3b, v14
	v_exp_f32_e32 v38, v15
	v_fmamk_f32 v15, v9, 0x3db8aa3b, v14
	v_exp_f32_e32 v40, v15
	v_fmamk_f32 v15, v10, 0x3db8aa3b, v14
	v_exp_f32_e32 v97, v15
	v_fmamk_f32 v15, v11, 0x3db8aa3b, v14
	v_exp_f32_e32 v103, v15
	v_fmamk_f32 v15, v12, 0x3db8aa3b, v14
	v_exp_f32_e32 v45, v15
	v_fmamk_f32 v15, v13, 0x3db8aa3b, v14
	v_exp_f32_e32 v101, v15
	v_fmamk_f32 v15, v2, 0x3db8aa3b, v14
	v_exp_f32_e32 v43, v15
	v_fmamk_f32 v15, v3, 0x3db8aa3b, v14
	v_exp_f32_e32 v99, v15
	v_fmamk_f32 v15, v4, 0x3db8aa3b, v14
	v_exp_f32_e32 v39, v15
	v_fmac_f32_e32 v14, 0x3db8aa3b, v5
	v_exp_f32_e32 v41, v14
	v_pk_add_f32 v[14:15], v[96:97], 0 op_sel_hi:[1,0]
	v_pk_add_f32 v[16:17], v[42:43], 0 op_sel_hi:[1,0]
	v_pk_add_f32 v[14:15], v[14:15], v[102:103]
	v_pk_add_f32 v[16:17], v[16:17], v[98:99]
	v_pk_add_f32 v[14:15], v[14:15], v[44:45]
	v_pk_add_f32 v[16:17], v[16:17], v[38:39]
	v_pk_add_f32 v[14:15], v[14:15], v[100:101]
	v_pk_add_f32 v[16:17], v[16:17], v[40:41]
	v_mul_f32_e32 v116, 0x3d800000, v115
	v_pk_add_f32 v[14:15], v[14:15], v[16:17]
	v_mul_f32_e32 v113, v113, v114
	v_add_f32_e32 v16, v14, v15
	v_mov_b32_e32 v14, v106
	v_mov_b32_e32 v15, v10
	v_pk_fma_f32 v[14:15], v[96:97], v[14:15], 0 op_sel_hi:[1,1,0]
	v_mov_b32_e32 v10, v107
	v_pk_fma_f32 v[10:11], v[102:103], v[10:11], v[14:15]
	v_mov_b32_e32 v14, v108
	v_mov_b32_e32 v15, v12
	v_pk_fma_f32 v[10:11], v[44:45], v[14:15], v[10:11]
	v_mov_b32_e32 v12, v109
	v_pk_fma_f32 v[10:11], v[100:101], v[12:13], v[10:11]
	v_mov_b32_e32 v12, v6
	v_mov_b32_e32 v13, v2
	v_pk_fma_f32 v[12:13], v[42:43], v[12:13], 0 op_sel_hi:[1,1,0]
	v_mov_b32_e32 v2, v7
	v_pk_fma_f32 v[2:3], v[98:99], v[2:3], v[12:13]
	v_mov_b32_e32 v6, v8
	v_mov_b32_e32 v7, v4
	v_pk_fma_f32 v[2:3], v[38:39], v[6:7], v[2:3]
	v_rcp_f32_e32 v6, v16
	v_mov_b32_e32 v4, v9
	v_pk_fma_f32 v[2:3], v[40:41], v[4:5], v[2:3]
	v_mul_f32_e32 v108, v55, v6
	v_pk_add_f32 v[2:3], v[10:11], v[2:3]
	v_mul_f32_e32 v117, v16, v108
	v_add_f32_e32 v2, v2, v3
	v_mul_f32_e32 v109, v2, v108
	v_mul_f32_e32 v106, 0x3d800000, v109
	v_max3_f32 v34, v112, v116, v106
	v_mov_b32_e32 v36, v34
	s_nop 1
	v_permlane16_swap_b32_e32 v34, v36
	v_max_f32_e32 v36, v36, v36
	v_max_f32_e32 v34, v34, v34
	v_max_f32_e32 v34, v34, v36
	v_mov_b32_e32 v36, v34
	s_nop 1
	v_permlane32_swap_b32_e32 v34, v36
	v_max_f32_e32 v36, v36, v36
	v_max_f32_e32 v34, v34, v34
	v_max_f32_e32 v36, v34, v36
	v_fma_f32 v34, v111, s6, -v36
	v_mul_f32_e32 v34, 0x3fb8aa3b, v34
	v_exp_f32_e32 v34, v34
	v_mov_b32_e32 v106, v35
	v_mov_b32_e32 v107, v35
	v_cmp_gt_u32_e32 vcc, 16, v104
	v_mul_f32_e32 v37, v110, v34
	v_mul_f32_e32 v37, 0x43800000, v37
	v_mul_f32_e32 v55, v37, v76
	v_mul_f32_e32 v76, v37, v78
	v_cvt_pk_fp8_f32 v106, v55, v76
	v_mul_f32_e32 v52, v37, v52
	v_mul_f32_e32 v55, v37, v74
	v_mul_f32_e32 v50, v37, v50
	v_cvt_pk_fp8_f32 v106, v52, v55 op_sel:[0,0,1]
	v_mul_f32_e32 v52, v37, v72
	v_cvt_pk_fp8_f32 v107, v50, v52
	v_mul_f32_e32 v52, v37, v77
	v_mul_f32_e32 v55, v37, v79
	v_mov_b32_e32 v50, v35
	v_cvt_pk_fp8_f32 v50, v52, v55
	v_mul_f32_e32 v48, v37, v48
	v_mul_f32_e32 v46, v37, v46
	v_cvt_pk_fp8_f32 v107, v48, v46 op_sel:[0,0,1]
	v_mul_f32_e32 v46, v37, v53
	v_mul_f32_e32 v48, v37, v75
	v_cvt_pk_fp8_f32 v50, v46, v48 op_sel:[0,0,1]
	v_mul_f32_e32 v46, v37, v51
	v_mul_f32_e32 v48, v37, v73
	v_mov_b32_e32 v51, v35
	v_cvt_pk_fp8_f32 v51, v46, v48
	v_fma_f32 v48, v115, s6, -v36
	v_mul_f32_e32 v48, 0x3fb8aa3b, v48
	v_exp_f32_e32 v55, v48
	v_mul_f32_e32 v46, v37, v49
	v_mul_f32_e32 v37, v37, v47
	v_cvt_pk_fp8_f32 v51, v46, v37 op_sel:[0,0,1]
	s_waitcnt vmcnt(14)
	v_mfma_f32_16x16x32_fp8_fp8 v[46:49], v[106:107], v[30:31], 0
	v_mul_f32_e32 v30, v114, v55
	v_mul_f32_e32 v37, 0x43800000, v30
	v_mul_f32_e32 v30, v37, v92
	v_mul_f32_e32 v31, v37, v94
	v_mov_b32_e32 v52, v35
	v_cvt_pk_fp8_f32 v52, v30, v31
	v_mfma_f32_16x16x32_fp8_fp8 v[30:33], v[50:51], v[32:33], v[46:49]
	v_mov_b32_e32 v53, v35
	v_fma_f32 v50, v105, v34, 0
	v_fmac_f32_e32 v50, v113, v55
	v_mul_f32_e32 v46, v37, v84
	v_mul_f32_e32 v47, v37, v90
	v_cvt_pk_fp8_f32 v52, v46, v47 op_sel:[0,0,1]
	v_mul_f32_e32 v46, v37, v82
	v_mul_f32_e32 v47, v37, v88
	v_cvt_pk_fp8_f32 v53, v46, v47
	v_mul_f32_e32 v47, v37, v93
	v_mul_f32_e32 v48, v37, v95
	v_mov_b32_e32 v46, v35
	v_cvt_pk_fp8_f32 v46, v47, v48
	v_mul_f32_e32 v47, v37, v80
	v_mul_f32_e32 v48, v37, v86
	v_cvt_pk_fp8_f32 v53, v47, v48 op_sel:[0,0,1]
	v_mul_f32_e32 v47, v37, v85
	v_mul_f32_e32 v48, v37, v91
	v_cvt_pk_fp8_f32 v46, v47, v48 op_sel:[0,0,1]
	v_mul_f32_e32 v48, v37, v83
	v_mul_f32_e32 v49, v37, v89
	v_mov_b32_e32 v47, v35
	v_cvt_pk_fp8_f32 v47, v48, v49
	v_mul_f32_e32 v48, v37, v81
	v_mul_f32_e32 v37, v37, v87
	s_waitcnt vmcnt(12)
	v_mfma_f32_16x16x32_fp8_fp8 v[30:33], v[52:53], v[26:27], v[30:33]
	v_cvt_pk_fp8_f32 v47, v48, v37 op_sel:[0,0,1]
	v_fma_f32 v26, v109, s6, -v36
	v_mul_f32_e32 v26, 0x3fb8aa3b, v26
	v_exp_f32_e32 v51, v26
	v_mfma_f32_16x16x32_fp8_fp8 v[26:29], v[46:47], v[28:29], v[30:33]
	s_nop 2
	v_mul_f32_e32 v30, v108, v51
	v_mul_f32_e32 v32, 0x43800000, v30
	v_mul_f32_e32 v31, v32, v96
	v_mul_f32_e32 v33, v32, v102
	v_mov_b32_e32 v30, v35
	v_cvt_pk_fp8_f32 v30, v31, v33
	v_mul_f32_e32 v33, v32, v44
	v_mul_f32_e32 v42, v32, v42
	v_mul_f32_e32 v44, v32, v98
	v_mov_b32_e32 v31, v35
	v_cvt_pk_fp8_f32 v31, v42, v44
	v_mul_f32_e32 v49, v105, v34
	v_add_f32_e32 v34, 0, v34
	v_add_f32_e32 v52, v34, v55
	v_mul_f32_e32 v34, v32, v100
	v_cvt_pk_fp8_f32 v30, v33, v34 op_sel:[0,0,1]
	v_mul_f32_e32 v33, v32, v38
	v_mul_f32_e32 v34, v32, v40
	v_cvt_pk_fp8_f32 v31, v33, v34 op_sel:[0,0,1]
	v_mul_f32_e32 v33, v32, v97
	v_mul_f32_e32 v38, v32, v103
	v_mov_b32_e32 v34, v35
	v_cvt_pk_fp8_f32 v34, v33, v38
	v_mul_f32_e32 v40, v32, v43
	v_mul_f32_e32 v42, v32, v99
	v_cvt_pk_fp8_f32 v35, v40, v42
	v_mul_f32_e32 v33, v32, v45
	v_mul_f32_e32 v38, v32, v101
	v_cvt_pk_fp8_f32 v34, v33, v38 op_sel:[0,0,1]
	v_mul_f32_e32 v33, v32, v39
	v_mul_f32_e32 v32, v32, v41
	v_cvt_pk_fp8_f32 v35, v33, v32 op_sel:[0,0,1]
	s_waitcnt vmcnt(10)
	v_mfma_f32_16x16x32_fp8_fp8 v[26:29], v[30:31], v[18:19], v[26:29]
	v_fma_mix_f32 v37, v49, v70, 0 op_sel_hi:[0,1,0]
	v_mul_f32_e32 v32, v113, v55
	v_fma_mix_f32 v48, v49, v70, 0 op_sel:[0,1,0] op_sel_hi:[0,1,0]
	v_fma_mix_f32 v33, v32, v66, v37 op_sel_hi:[0,1,0]
	v_mfma_f32_16x16x32_fp8_fp8 v[18:21], v[34:35], v[20:21], v[26:29]
	v_fma_mix_f32 v30, v32, v66, v48 op_sel:[0,1,0] op_sel_hi:[0,1,0]
	s_nop 1
	v_mul_f32_e32 v26, v117, v51
	s_waitcnt vmcnt(9)
	v_fma_mix_f32 v27, v26, v68, v33 op_sel_hi:[0,1,0]
	v_fma_mix_f32 v29, v26, v68, v30 op_sel:[0,1,0] op_sel_hi:[0,1,0]
	v_mov_b32_e32 v30, v27
	v_fma_mix_f32 v49, v49, v71, 0 op_sel_hi:[0,1,0]
	s_nop 0
	v_permlane16_swap_b32_e32 v27, v30
	v_fma_mix_f32 v31, v32, v67, v49 op_sel_hi:[0,1,0]
	v_add_f32_e32 v32, v52, v51
	v_add_f32_e32 v30, v27, v30
	v_mov_b32_e32 v27, v29
	v_fma_mix_f32 v37, v26, v69, v31 op_sel_hi:[0,1,0]
	v_mov_b32_e32 v26, v32
	v_permlane16_swap_b32_e32 v29, v27
	v_fmac_f32_e32 v50, v117, v51
	v_permlane16_swap_b32_e32 v32, v26
	v_add_f32_e32 v31, v29, v27
	v_mov_b32_e32 v27, v37
	v_add_f32_e32 v34, v32, v26
	v_mov_b32_e32 v26, v50
	v_permlane16_swap_b32_e32 v37, v27
	s_nop 0
	v_permlane16_swap_b32_e32 v50, v26
	v_add_f32_e32 v27, v37, v27
	v_mul_u32_u24_e32 v37, 0x140, v1
	s_movk_i32 s6, 0x500
	v_add_f32_e32 v26, v50, v26
	v_mad_u32_u24 v37, v63, s6, v37
	v_mov_b32_e32 v35, v34
	v_mov_b32_e32 v28, v26
	v_mov_b32_e32 v32, v30
	v_mov_b32_e32 v33, v31
	v_mov_b32_e32 v29, v27
	v_lshl_or_b32 v37, v57, 2, v37
	v_permlane32_swap_b32_e32 v34, v35
	v_permlane32_swap_b32_e32 v26, v28
	v_permlane32_swap_b32_e32 v30, v32
	v_permlane32_swap_b32_e32 v31, v33
	v_permlane32_swap_b32_e32 v27, v29
	v_add_u32_e32 v37, 0x1c00, v37
	s_mov_b64 s[24:25], 0
	s_mov_b64 s[6:7], 0
	ds_write2_b32 v37, v18, v19 offset1:20
	ds_write2_b32 v37, v20, v21 offset0:40 offset1:60
	s_and_saveexec_b64 s[26:27], vcc
	s_mov_b64 s[6:7], exec
	v_pk_add_f32 v[18:19], v[30:31], v[32:33]
	v_pk_add_f32 v[20:21], v[26:27], v[28:29]
	v_add_f32_e32 v37, v34, v35
	s_or_b64 exec, exec, s[26:27]
	s_branch .LBB1_30
.LBB1_16:
	s_mov_b32 exec_lo, 0x1ff01ff
	s_mov_b32 exec_hi, 0x1ff01ff
	global_load_dword v120, v144, s[10:11]
	s_mov_b32 exec_lo, 0xe000e00
	s_mov_b32 exec_hi, 0xe000e00
	global_load_dword v120, v145, s[12:13]
	s_mov_b32 exec_lo, 0x70007000
	s_mov_b32 exec_hi, 0x70007000
	global_load_dword v120, v146, s[14:15]
	s_mov_b64 exec, -1
	global_load_dwordx4 v[124:127], v147, s[22:23]
	global_load_dwordx4 v[128:131], v148, s[22:23]
	s_mov_b32 exec_hi, 0
	global_load_dwordx4 v[132:135], v149, s[16:17]
	s_mov_b32 exec_hi, -1
	s_mov_b32 exec_lo, 0
	global_load_dwordx4 v[132:135], v149, s[18:19] offset:-512
	s_mov_b32 exec_lo, -1
	global_load_dwordx4 v[136:139], v150, s[8:9]
	global_load_dwordx4 v[140:143], v150, s[8:9] offset:256
	s_movk_i32 s6, 0x140
	v_cmp_gt_u32_e32 vcc, s6, v0
	v_lshlrev_b32_e32 v18, 2, v0
	v_mov_b32_e32 v19, 0
	s_and_saveexec_b64 s[6:7], vcc
	ds_write_b32 v18, v19 offset:14336
	s_or_b64 exec, exec, s[6:7]
	v_cmp_gt_u32_e32 vcc, 64, v0
	s_and_saveexec_b64 s[6:7], vcc
	ds_write_b32 v18, v19 offset:15360
	s_or_b64 exec, exec, s[6:7]
	v_mul_u32_u24_e32 v18, 0x140, v1
	s_movk_i32 s6, 0x500
	v_mad_u32_u24 v18, v63, s6, v18
	v_lshl_or_b32 v18, v57, 2, v18
	v_mov_b32_e32 v21, 0
	v_add_u32_e32 v18, 0x1c00, v18
	ds_write2_b32 v18, v21, v21 offset1:20
	ds_write2_b32 v18, v21, v21 offset0:40 offset1:60
	v_cmp_gt_u32_e64 s[6:7], 16, v104
	v_mov_b32_e32 v37, 1.0
	v_mov_b32_e32 v20, 0
	v_mov_b32_e32 v19, 0
	v_mov_b32_e32 v18, 0
	v_mov_b32_e32 v36, 0

.LBB1_36:
	s_or_b64 exec, exec, s[10:11]
	v_fma_f32 v34, v21, v36, 0
	s_waitcnt lgkmcnt(1)
	v_fma_f32 v35, v21, v38, 0
	v_fmac_f32_e32 v34, v29, v28
	v_fmac_f32_e32 v35, v29, v39
	v_fmac_f32_e32 v34, v30, v32
	s_waitcnt lgkmcnt(0)
	v_fmac_f32_e32 v35, v30, v26
	v_fmac_f32_e32 v34, v33, v20
	v_fmac_f32_e32 v35, v33, v27
	s_waitcnt vmcnt(6)
	v_mov_b32_dpp v33, v120 row_newbcast:10 row_mask:0xf bank_mask:0xf bound_ctrl:1
	v_mov_b32_dpp v36, v120 row_newbcast:11 row_mask:0xf bank_mask:0xf bound_ctrl:1
	v_cmp_eq_u32_e64 s[10:11], 1, v57
	v_mov_b32_dpp v32, v120 row_newbcast:9 row_mask:0xf bank_mask:0xf bound_ctrl:1
	v_mov_b32_dpp v38, v120 row_newbcast:13 row_mask:0xf bank_mask:0xf bound_ctrl:1
	v_mov_b32_dpp v39, v120 row_newbcast:14 row_mask:0xf bank_mask:0xf bound_ctrl:1
	v_cndmask_b32_e64 v33, v36, v33, s[10:11]
	v_cmp_eq_u32_e64 s[8:9], 0, v57
	v_mov_b32_dpp v37, v120 row_newbcast:12 row_mask:0xf bank_mask:0xf bound_ctrl:1
	v_mov_b32_dpp v27, v120 row_newbcast:0 row_mask:0xf bank_mask:0xf bound_ctrl:1
	v_cndmask_b32_e64 v32, v33, v32, s[8:9]
	v_cndmask_b32_e64 v33, v39, v38, s[10:11]
	v_cndmask_b32_e64 v33, v33, v37, s[8:9]
	v_fma_f32 v33, v34, v33, -v35
	v_fma_f32 v32, v18, v33, -v32
	v_mov_b32_dpp v20, v120 row_newbcast:1 row_mask:0xf bank_mask:0xf bound_ctrl:1
	v_mov_b32_dpp v19, v120 row_newbcast:2 row_mask:0xf bank_mask:0xf bound_ctrl:1
	v_mov_b32_dpp v31, v120 row_newbcast:3 row_mask:0xf bank_mask:0xf bound_ctrl:1
	v_mov_b32_dpp v29, v120 row_newbcast:4 row_mask:0xf bank_mask:0xf bound_ctrl:1
	v_mov_b32_dpp v26, v120 row_newbcast:5 row_mask:0xf bank_mask:0xf bound_ctrl:1
	v_mov_b32_dpp v30, v120 row_newbcast:6 row_mask:0xf bank_mask:0xf bound_ctrl:1
	v_mov_b32_dpp v28, v120 row_newbcast:7 row_mask:0xf bank_mask:0xf bound_ctrl:1
	v_mov_b32_dpp v21, v120 row_newbcast:8 row_mask:0xf bank_mask:0xf bound_ctrl:1
	v_mov_b32_dpp v18, v32 quad_perm:[0,0,0,0] row_mask:0xf bank_mask:0xf bound_ctrl:1
	v_mov_b32_dpp v33, v32 quad_perm:[1,1,1,1] row_mask:0xf bank_mask:0xf bound_ctrl:1
	v_mov_b32_dpp v32, v32 quad_perm:[2,2,2,2] row_mask:0xf bank_mask:0xf bound_ctrl:1
	s_and_b64 s[12:13], vcc, s[4:5]
	s_and_b64 exec, exec, s[12:13]
	s_cbranch_execz .LBB1_39
	v_mul_f32_e32 v31, v31, v33
	v_fmac_f32_e32 v31, v27, v18
	v_mul_f32_e32 v27, v29, v33
	v_fmac_f32_e32 v27, v20, v18
	v_fmac_f32_e32 v27, v28, v32
	v_mul_f32_e32 v20, v26, v33
	v_fmac_f32_e32 v31, v30, v32
	v_fmac_f32_e32 v20, v19, v18
	v_mul_f32_e32 v18, v27, v27
	v_fmac_f32_e32 v20, v21, v32
	v_fmac_f32_e32 v18, v31, v31
	v_fmac_f32_e32 v18, v20, v20
	s_mov_b32 s12, 0xf800000
	v_mul_f32_e32 v19, 0x4f800000, v18
	v_cmp_gt_f32_e32 vcc, s12, v18
	s_nop 1
	v_cndmask_b32_e32 v18, v18, v19, vcc
	v_sqrt_f32_e32 v19, v18
	s_nop 0
	v_add_u32_e32 v21, -1, v19
	v_fma_f32 v26, -v21, v19, v18
	v_cmp_ge_f32_e64 s[12:13], 0, v26
	v_add_u32_e32 v26, 1, v19
	s_nop 0
	v_cndmask_b32_e64 v21, v19, v21, s[12:13]
	v_fma_f32 v19, -v26, v19, v18
	v_cmp_lt_f32_e64 s[12:13], 0, v19
	s_nop 1
	v_cndmask_b32_e64 v19, v21, v26, s[12:13]
	v_mul_f32_e32 v21, 0x37800000, v19
	v_cndmask_b32_e32 v19, v19, v21, vcc
	v_mov_b32_e32 v21, 0x260
	v_cmp_class_f32_e32 vcc, v18, v21
	s_nop 1
	v_cndmask_b32_e32 v18, v19, v18, vcc
	v_add_f32_e32 v19, 0x38d1b717, v18
	v_div_scale_f32 v21, s[12:13], v19, v19, 1.0
	v_rcp_f32_e32 v26, v21
	s_nop 0
	v_fma_f32 v28, -v21, v26, 1.0
	v_fmac_f32_e32 v26, v28, v26
	v_div_scale_f32 v28, vcc, 1.0, v19, 1.0
	v_mul_f32_e32 v29, v28, v26
	v_fma_f32 v30, -v21, v29, v28
	v_fmac_f32_e32 v29, v30, v26
	v_fma_f32 v21, -v21, v29, v28
	v_div_fmas_f32 v21, v21, v26, v29
	v_div_fixup_f32 v21, v21, v19, 1.0
	v_cndmask_b32_e64 v19, v20, v27, s[10:11]
	v_mad_u32_u24 v26, v56, 3, v57
	v_cndmask_b32_e64 v20, v19, v31, s[8:9]
	v_mul_lo_u16_e32 v19, 37, v26
	v_sub_u16_sdwa v28, v26, v19 dst_sel:DWORD dst_unused:UNUSED_PAD src0_sel:DWORD src1_sel:BYTE_1
	v_lshrrev_b16_e32 v28, 1, v28
	v_and_b32_e32 v28, 0x7f, v28
	v_add_u16_sdwa v19, v28, v19 dst_sel:DWORD dst_unused:UNUSED_PAD src0_sel:DWORD src1_sel:BYTE_1
	v_lshrrev_b16_e32 v19, 2, v19
	v_and_b32_e32 v19, 63, v19
	v_cvt_f16_f32_e32 v27, v20
	v_and_b32_e32 v28, 0xffff, v19
	v_mul_lo_u16_e32 v19, 7, v19
	v_sub_u16_e32 v29, v26, v19
	v_mov_b32_e32 v19, 1
	v_lshlrev_b32_sdwa v29, v19, v29 dst_sel:DWORD dst_unused:UNUSED_PAD src0_sel:DWORD src1_sel:BYTE_0
	s_movk_i32 s10, 0x50
	v_mad_u32_u24 v28, v28, s10, v29
	ds_write_b16 v28, v27 offset:14368
	v_mov_b32_e32 v27, 0x818
	v_fma_mixlo_f16 v20, v20, v21, 0
	v_add_u16_e32 v21, 56, v26
	v_mad_legacy_u16 v26, v26, 37, v27
	v_sub_u16_sdwa v27, v21, v26 dst_sel:DWORD dst_unused:UNUSED_PAD src0_sel:DWORD src1_sel:BYTE_1
	v_lshrrev_b16_e32 v27, 1, v27
	v_and_b32_e32 v27, 0x7f, v27
	v_add_u16_sdwa v26, v27, v26 dst_sel:DWORD dst_unused:UNUSED_PAD src0_sel:DWORD src1_sel:BYTE_1
	v_lshrrev_b16_e32 v26, 2, v26
	v_and_b32_e32 v26, 63, v26
	v_and_b32_e32 v27, 0xffff, v26
	v_mul_lo_u16_e32 v26, 7, v26
	v_sub_u16_e32 v21, v21, v26
	v_lshlrev_b32_sdwa v21, v19, v21 dst_sel:DWORD dst_unused:UNUSED_PAD src0_sel:DWORD src1_sel:BYTE_0
	v_mad_u32_u24 v21, v27, s10, v21
	ds_write_b16 v21, v20 offset:14368
	s_and_b64 exec, exec, s[8:9]
	s_cbranch_execz .LBB1_39
	v_add_u16_e32 v20, 42, v56
	v_mul_lo_u16_e32 v21, 37, v20
	v_lshrrev_b16_e32 v21, 8, v21
	v_cvt_f16_f32_e32 v18, v18
	v_mul_lo_u16_e32 v26, 7, v21
	v_sub_u16_e32 v20, v20, v26
	v_lshlrev_b32_sdwa v19, v19, v20 dst_sel:DWORD dst_unused:UNUSED_PAD src0_sel:DWORD src1_sel:BYTE_0
	v_mad_u32_u24 v19, v21, s10, v19
	ds_write_b16 v19, v18 offset:14368
.LBB1_39:
	s_or_b64 exec, exec, s[14:15]
	s_load_dwordx2 s[14:15], s[0:1], 0x38
	v_cmp_eq_u32_e32 vcc, 3, v63
	s_and_saveexec_b64 s[0:1], vcc
	s_cbranch_execz .LBB1_41
	v_lshlrev_b32_e32 v18, 4, v104
	s_waitcnt vmcnt(2)
	ds_write_b128 v18, v[132:135] offset:15616
.LBB1_41:
	s_or_b64 exec, exec, s[0:1]
	s_movk_i32 s0, 0x200
	v_cmp_gt_u32_e32 vcc, s0, v0
	s_waitcnt lgkmcnt(0)
	s_barrier
	s_and_saveexec_b64 s[16:17], vcc
	s_cbranch_execz .LBB1_51
	v_mul_u32_u24_e32 v18, 0x50, v57
	v_lshl_add_u32 v18, v58, 1, v18
	ds_read_b128 v[18:21], v18 offset:14336
	s_waitcnt vmcnt(2)
	v_lshlrev_b32_e32 v23, 2, v57
	v_lshlrev_b32_e32 v24, 2, v1
	v_and_b32_e32 v22, 0xc0, v0
	v_lshlrev_b32_e32 v25, 11, v1
	v_or3_b32 v25, v23, v22, v25
	v_lshrrev_b32_e64 v22, v24, s3
	v_bfe_u32 v26, s3, v24, 1
	v_and_b32_e32 v27, 2, v22
	s_waitcnt lgkmcnt(0)
	v_mfma_f32_16x16x32_f16 v[14:17], v[18:21], v[124:127], 0
	v_cmp_eq_u32_e32 vcc, 0, v26
	v_cmp_eq_u32_e64 s[0:1], 0, v27
	v_cmp_ne_u32_e64 s[8:9], 3, v1
	s_nop 4
	v_cndmask_b32_e64 v14, v14, 0, vcc
	v_cndmask_b32_e64 v15, v15, 0, s[0:1]
	ds_write2st64_b32 v25, v14, v15 offset1:2
	s_and_saveexec_b64 s[12:13], s[8:9]
	v_and_b32_e32 v1, 4, v22
	v_cmp_ne_u32_e64 s[10:11], 0, v1
	s_nop 1
	v_cndmask_b32_e64 v1, 0, v16, s[10:11]
	ds_write_b32 v25, v1 offset:1024
	s_or_b64 exec, exec, s[12:13]
	v_or_b32_e32 v1, 3, v24
	v_cmp_gt_u32_e64 s[10:11], 14, v1
	s_and_saveexec_b64 s[18:19], s[10:11]
	v_and_b32_e32 v1, 8, v22
	v_cmp_ne_u32_e64 s[12:13], 0, v1
	s_nop 1
	v_cndmask_b32_e64 v1, 0, v17, s[12:13]
	ds_write_b32 v25, v1 offset:1536
	s_or_b64 exec, exec, s[18:19]
	s_and_b64 exec, exec, s[6:7]
	s_cbranch_execz .LBB1_51
	v_mfma_f32_16x16x32_f16 v[6:9], v[18:21], v[128:131], 0
	v_and_b32_e32 v0, 0xc0, v0
	v_lshlrev_b32_e32 v1, 9, v24
	v_or3_b32 v0, v23, v0, v1
	s_nop 4
	v_cndmask_b32_e64 v1, v6, 0, vcc
	v_cndmask_b32_e64 v6, v7, 0, s[0:1]
	ds_write2st64_b32 v0, v1, v6 offset0:1 offset1:3
	s_and_saveexec_b64 s[0:1], s[8:9]
	v_and_b32_e32 v1, 4, v22
	v_cmp_ne_u32_e32 vcc, 0, v1
	s_nop 1
	v_cndmask_b32_e32 v1, 0, v8, vcc
	ds_write_b32 v0, v1 offset:1280
	s_or_b64 exec, exec, s[0:1]
	s_and_b64 exec, exec, s[10:11]
	v_and_b32_e32 v1, 8, v22
	v_cmp_ne_u32_e32 vcc, 0, v1
	s_nop 1
	v_cndmask_b32_e32 v1, 0, v9, vcc
	ds_write_b32 v0, v1 offset:1792
.LBB1_51:
	s_or_b64 exec, exec, s[16:17]
	s_waitcnt lgkmcnt(0)
	s_barrier
	s_and_saveexec_b64 s[0:1], s[4:5]
	s_cbranch_execz .LBB1_53
	v_lshl_or_b32 v0, v56, 9, v54
	s_waitcnt vmcnt(3)
	ds_read_b128 v[6:9], v0 offset:256
	ds_read_b128 v[14:17], v0
	s_mov_b32 s0, 0x800000
	v_mov_b32_e32 v55, 0
	s_waitcnt vmcnt(0) lgkmcnt(1)
	v_pk_add_f32 v[0:1], v[140:141], v[6:7]
	s_waitcnt lgkmcnt(0)
	v_pk_add_f32 v[2:3], v[136:137], v[14:15]
	v_pk_add_f32 v[6:7], v[142:143], v[8:9]
	v_pk_add_f32 v[4:5], v[138:139], v[16:17]
	v_mov_b32_e32 v8, v2
	v_mov_b32_e32 v9, v0
	v_mov_b32_e32 v10, v3
	v_mov_b32_e32 v11, v1
	v_pk_add_f32 v[8:9], v[8:9], v[10:11]
	v_mov_b32_e32 v10, v4
	v_mov_b32_e32 v11, v6
	v_mov_b32_e32 v12, v5
	v_mov_b32_e32 v13, v7
	v_pk_add_f32 v[10:11], v[10:11], v[12:13]
	s_nop 0
	v_pk_add_f32 v[8:9], v[8:9], v[10:11]
	s_nop 0
	v_add_f32_e32 v8, v8, v9
	s_nop 1
	v_add_f32_dpp v8, v8, v8 quad_perm:[1,0,3,2] row_mask:0xf bank_mask:0xf bound_ctrl:1
	s_nop 1
	v_add_f32_dpp v8, v8, v8 quad_perm:[2,3,0,1] row_mask:0xf bank_mask:0xf bound_ctrl:1
	s_nop 1
	v_add_f32_dpp v8, v8, v8 row_half_mirror row_mask:0xf bank_mask:0xf bound_ctrl:1
	s_nop 1
	v_add_f32_dpp v8, v8, v8 row_mirror row_mask:0xf bank_mask:0xf bound_ctrl:1
	v_mul_f32_e32 v8, 0x3c000000, v8
	v_pk_add_f32 v[16:17], v[2:3], v[8:9] op_sel_hi:[1,0] neg_lo:[0,1] neg_hi:[0,1]
	v_pk_add_f32 v[18:19], v[0:1], v[8:9] op_sel_hi:[1,0] neg_lo:[0,1] neg_hi:[0,1]
	v_mov_b32_e32 v0, v16
	v_mov_b32_e32 v1, v18
	v_pk_add_f32 v[20:21], v[4:5], v[8:9] op_sel_hi:[1,0] neg_lo:[0,1] neg_hi:[0,1]
	v_pk_add_f32 v[22:23], v[6:7], v[8:9] op_sel_hi:[1,0] neg_lo:[0,1] neg_hi:[0,1]
	v_pk_fma_f32 v[0:1], v[0:1], v[0:1], 0 op_sel_hi:[1,1,0]
	v_mov_b32_e32 v2, v17
	v_mov_b32_e32 v3, v19
	v_pk_fma_f32 v[0:1], v[2:3], v[2:3], v[0:1]
	v_mov_b32_e32 v2, v20
	v_mov_b32_e32 v3, v22
	v_pk_fma_f32 v[0:1], v[2:3], v[2:3], v[0:1]
	v_mov_b32_e32 v2, v21
	v_mov_b32_e32 v3, v23
	v_pk_fma_f32 v[0:1], v[2:3], v[2:3], v[0:1]
	s_nop 0
	v_add_f32_e32 v0, v0, v1
	v_mov_b32_e32 v1, 0x3727c5ac
	s_nop 0
	v_add_f32_dpp v0, v0, v0 quad_perm:[1,0,3,2] row_mask:0xf bank_mask:0xf bound_ctrl:1
	s_nop 1
	v_add_f32_dpp v0, v0, v0 quad_perm:[2,3,0,1] row_mask:0xf bank_mask:0xf bound_ctrl:1
	s_nop 1
	v_add_f32_dpp v0, v0, v0 row_half_mirror row_mask:0xf bank_mask:0xf bound_ctrl:1
	s_nop 1
	v_add_f32_dpp v0, v0, v0 row_mirror row_mask:0xf bank_mask:0xf bound_ctrl:1
	v_fmac_f32_e32 v1, 0x3c000000, v0
	v_mul_f32_e32 v0, 0x4b800000, v1
	v_cmp_gt_f32_e32 vcc, s0, v1
	s_nop 1
	v_cndmask_b32_e32 v0, v1, v0, vcc
	v_rsq_f32_e32 v24, v0
	ds_read_b128 v[0:3], v54 offset:15872
	ds_read_b128 v[4:7], v54 offset:15616
	ds_read_b128 v[8:11], v54 offset:16384
	ds_read_b128 v[12:15], v54 offset:16128
	v_mul_f32_e32 v25, 0x45800000, v24
	v_cndmask_b32_e32 v24, v24, v25, vcc
	v_pk_mul_f32 v[16:17], v[16:17], v[24:25] op_sel_hi:[1,0]
	v_pk_mul_f32 v[20:21], v[20:21], v[24:25] op_sel_hi:[1,0]
	s_waitcnt lgkmcnt(0)
	v_pk_fma_f32 v[4:5], v[4:5], v[16:17], v[12:13]
	v_pk_mul_f32 v[12:13], v[18:19], v[24:25] op_sel_hi:[1,0]
	v_pk_fma_f32 v[6:7], v[6:7], v[20:21], v[14:15]
	v_pk_fma_f32 v[0:1], v[0:1], v[12:13], v[8:9]
	v_mad_u64_u32 v[8:9], s[0:1], s2, 14, v[56:57]
	v_ashrrev_i32_e32 v9, 31, v8
	v_lshlrev_b64 v[8:9], 9, v[8:9]
	v_lshl_add_u64 v[8:9], s[14:15], 0, v[8:9]
	v_pk_mul_f32 v[14:15], v[22:23], v[24:25] op_sel_hi:[1,0]
	v_lshl_add_u64 v[8:9], v[8:9], 0, v[54:55]
	v_pk_fma_f32 v[2:3], v[2:3], v[14:15], v[10:11]
	global_store_dwordx4 v[8:9], v[4:7], off nt
	global_store_dwordx4 v[8:9], v[0:3], off offset:256 nt

	.amdhsa_kernel _Z11attn_kernelILi4EEvPKfS1_S1_S1_S1_S1_PKcPf
		.amdhsa_group_segment_fixed_size 16640
		.amdhsa_private_segment_fixed_size 0
		.amdhsa_kernarg_size 64
		.amdhsa_user_sgpr_count 2
		.amdhsa_user_sgpr_dispatch_ptr 0
		.amdhsa_user_sgpr_queue_ptr 0
		.amdhsa_user_sgpr_kernarg_segment_ptr 1
		.amdhsa_user_sgpr_dispatch_id 0
		.amdhsa_user_sgpr_kernarg_preload_length 0
		.amdhsa_user_sgpr_kernarg_preload_offset 0
		.amdhsa_user_sgpr_private_segment_size 0
		.amdhsa_uses_dynamic_stack 0
		.amdhsa_enable_private_segment 0
		.amdhsa_system_sgpr_workgroup_id_x 1
		.amdhsa_system_sgpr_workgroup_id_y 0
		.amdhsa_system_sgpr_workgroup_id_z 0
		.amdhsa_system_sgpr_workgroup_info 0
		.amdhsa_system_vgpr_workitem_id 0
		.amdhsa_next_free_vgpr 152
		.amdhsa_next_free_sgpr 32
		.amdhsa_accum_offset 152
		.amdhsa_reserve_vcc 1
		.amdhsa_float_round_mode_32 0
		.amdhsa_float_round_mode_16_64 0
		.amdhsa_float_denorm_mode_32 3
		.amdhsa_float_denorm_mode_16_64 3
		.amdhsa_dx10_clamp 1
		.amdhsa_ieee_mode 1
		.amdhsa_fp16_overflow 0
		.amdhsa_tg_split 0
		.amdhsa_exception_fp_ieee_invalid_op 0
		.amdhsa_exception_fp_denorm_src 0
		.amdhsa_exception_fp_ieee_div_zero 0
		.amdhsa_exception_fp_ieee_overflow 0
		.amdhsa_exception_fp_ieee_underflow 0
		.amdhsa_exception_fp_ieee_inexact 0
		.amdhsa_exception_int_div_zero 0
	.end_amdhsa_kernel

	.text
	.p2alignl 8, 3212836864
	.fill 256, 4, 3212836864

amdhsa.kernels:
  - .agpr_count:     12
    .args:
      - .actual_access:  read_only
        .address_space:  global
        .offset:         0
        .size:           8
        .value_kind:     global_buffer
      - .actual_access:  read_only
        .address_space:  global
        .offset:         8
        .size:           8
        .value_kind:     global_buffer
      - .actual_access:  read_only
        .address_space:  global
        .offset:         16
        .size:           8
        .value_kind:     global_buffer
      - .actual_access:  read_only
        .address_space:  global
        .offset:         24
        .size:           8
        .value_kind:     global_buffer
      - .actual_access:  read_only
        .address_space:  global
        .offset:         32
        .size:           8
        .value_kind:     global_buffer
      - .actual_access:  read_only
        .address_space:  global
        .offset:         40
        .size:           8
        .value_kind:     global_buffer
      - .actual_access:  read_only
        .address_space:  global
        .offset:         48
        .size:           8
        .value_kind:     global_buffer
      - .actual_access:  read_only
        .address_space:  global
        .offset:         56
        .size:           8
        .value_kind:     global_buffer
      - .actual_access:  read_only
        .address_space:  global
        .offset:         64
        .size:           8
        .value_kind:     global_buffer
      - .actual_access:  read_only
        .address_space:  global
        .offset:         72
        .size:           8
        .value_kind:     global_buffer
      - .actual_access:  write_only
        .address_space:  global
        .offset:         80
        .size:           8
        .value_kind:     global_buffer
    .group_segment_fixed_size: 13056
    .kernarg_segment_align: 8
    .kernarg_segment_size: 88
    .language:       OpenCL C
    .language_version:
      - 2
      - 0
    .max_flat_workgroup_size: 128
    .name:           _Z11prep_kernelPKfS0_PKiS2_S0_S0_S0_S0_S0_S0_Pc
    .private_segment_fixed_size: 0
    .sgpr_count:     38
    .sgpr_spill_count: 0
    .symbol:         _Z11prep_kernelPKfS0_PKiS2_S0_S0_S0_S0_S0_S0_Pc.kd
    .uniform_work_group_size: 1
    .uses_dynamic_stack: false
    .vgpr_count:     136
    .vgpr_spill_count: 0
    .wavefront_size: 64
  - .agpr_count:     0
    .args:
      - .actual_access:  read_only
        .address_space:  global
        .offset:         0
        .size:           8
        .value_kind:     global_buffer
      - .actual_access:  read_only
        .address_space:  global
        .offset:         8
        .size:           8
        .value_kind:     global_buffer
      - .actual_access:  read_only
        .address_space:  global
        .offset:         16
        .size:           8
        .value_kind:     global_buffer
      - .actual_access:  read_only
        .address_space:  global
        .offset:         24
        .size:           8
        .value_kind:     global_buffer
      - .actual_access:  read_only
        .address_space:  global
        .offset:         32
        .size:           8
        .value_kind:     global_buffer
      - .actual_access:  read_only
        .address_space:  global
        .offset:         40
        .size:           8
        .value_kind:     global_buffer
      - .actual_access:  read_only
        .address_space:  global
        .offset:         48
        .size:           8
        .value_kind:     global_buffer
      - .actual_access:  write_only
        .address_space:  global
        .offset:         56
        .size:           8
        .value_kind:     global_buffer
    .group_segment_fixed_size: 16640
    .kernarg_segment_align: 8
    .kernarg_segment_size: 64
    .language:       OpenCL C
    .language_version:
      - 2
      - 0
    .max_flat_workgroup_size: 256
    .name:           _Z11attn_kernelILi4EEvPKfS1_S1_S1_S1_S1_PKcPf
    .private_segment_fixed_size: 0
    .sgpr_count:     38
    .sgpr_spill_count: 0
    .symbol:         _Z11attn_kernelILi4EEvPKfS1_S1_S1_S1_S1_PKcPf.kd
    .uniform_work_group_size: 1
    .uses_dynamic_stack: false
    .vgpr_count:     152
    .vgpr_spill_count: 0
    .wavefront_size: 64
